# speedup vs baseline: 1.0424x; 1.0205x over previous
.LBB2_7:
	s_mov_b32 s24, 0
	s_andn2_b64 vcc, exec, s[4:5]
	v_mov_b32_e32 v81, 0
	s_cbranch_vccnz .LBB2_28
	s_cmp_gt_i32 s23, 12
	s_cbranch_scc1 .Lmy_dp_hi
	s_cmp_gt_i32 s23, 8
	s_cbranch_scc1 .Lmy_dp_mid
	s_setprio 0
	s_branch .Lmy_dp_done
.Lmy_dp_mid:
	s_setprio 1
	s_branch .Lmy_dp_done
.Lmy_dp_hi:
	s_cmp_gt_i32 s23, 16
	s_cbranch_scc1 .Lmy_dp_top
	s_setprio 2
	s_branch .Lmy_dp_done
.Lmy_dp_top:
	s_setprio 3
.Lmy_dp_done:
	s_waitcnt vmcnt(1)
	v_pk_add_f32 v[12:13], v[4:5], v[12:13]
	v_pk_add_f32 v[10:11], v[2:3], v[10:11]
	v_pk_mul_f32 v[16:17], v[12:13], s[14:15] op_sel_hi:[1,0]
	v_cmp_lt_f32_e32 vcc, 0, v12
	v_cndmask_b32_e64 v86, v65, v14, s[8:9]
	v_or_b32_e32 v74, 16, v62
	v_cndmask_b32_e32 v15, v16, v12, vcc
	v_cmp_lt_f32_e32 vcc, 0, v13
	v_lshlrev_b32_e32 v55, 12, v69
	v_lshlrev_b32_e32 v91, 5, v86
	v_cndmask_b32_e32 v14, v17, v13, vcc
	v_pk_mul_f32 v[12:13], v[10:11], s[14:15] op_sel_hi:[1,0]
	v_cmp_lt_f32_e32 vcc, 0, v10
	v_or_b32_e32 v93, v91, v62
	v_cmp_gt_u32_e64 s[4:5], 4, v62
	v_cndmask_b32_e32 v54, v12, v10, vcc
	v_cmp_lt_f32_e32 vcc, 0, v11
	v_mul_u32_u24_e32 v10, 20, v68
	v_mul_u32_u24_e32 v12, 0x280, v68
	v_cndmask_b32_e32 v16, v13, v11, vcc
	v_add_lshl_u32 v11, v10, v62, 5
	v_add_lshl_u32 v10, v10, v74, 5
	v_or_b32_e32 v96, v55, v12
	v_lshlrev_b32_e32 v72, 4, v62
	v_mov_b32_e32 v105, 0
	v_add_u32_e32 v98, v55, v11
	v_add_u32_e32 v99, v55, v10
	v_mov_b32_e32 v107, 0
	v_mov_b32_e32 v108, 0
	v_mov_b32_e32 v109, 0
	v_mov_b32_e32 v97, 0
	v_mov_b32_e32 v95, 0
	v_mov_b32_e32 v94, 0
	v_mov_b32_e32 v92, 0
	v_mov_b32_e32 v90, 0
	v_mov_b32_e32 v89, 0
	v_mov_b32_e32 v88, 0
	v_mov_b32_e32 v87, 0
	v_mov_b32_e32 v85, 0
	v_mov_b32_e32 v84, 0
	v_mov_b32_e32 v82, 0
	v_mov_b32_e32 v81, 0
	v_mov_b32_e32 v78, v77
	v_mov_b32_e32 v76, v77
	v_mov_b32_e32 v75, v77
	v_mov_b32_e32 v100, v77
	v_mov_b32_e32 v101, v77
	v_mov_b32_e32 v103, v77
	v_mov_b32_e32 v104, v77
